# union11 + attention tile loop: the rare near-tile bias block and the rare rescale block moved out of line (tests inverted), so the common far-tile path falls through instead of taking two branches per
# baseline (speedup 1.0000x reference)
.LBB0_397:
	s_add_i32 s0, s34, 0x80
	s_cmp_le_u32 s0, s24
	s_cselect_b64 s[78:79], -1, 0
	s_add_i32 s82, s31, 0
	s_add_i32 s3, s34, 0x13f
	s_cmp_gt_u32 s3, s16
	s_cselect_b64 s[36:37], -1, 0
	s_cmp_gt_u32 s0, s24
	s_cbranch_scc1 .Latt_noqk
	v_add_u32_e32 v152, s82, v164
	v_xor_b32_e32 v220, 32, v152
	v_xor_b32_e32 v221, 64, v152
	v_xor_b32_e32 v222, 0x60, v152
	ds_read_b128 v[204:207], v152
	ds_read_b128 v[208:211], v152 offset:4096
	ds_read_b128 v[212:215], v220
	ds_read_b128 v[216:219], v220 offset:4096
	s_add_i32 s0, s73, 0
	v_add_u32_e32 v196, s0, v171
	v_add_u32_e32 v197, s0, v170
	v_add_u32_e32 v202, s0, v169
	v_add_u32_e32 v203, s0, v168
	ds_read_b64_tr_b16 v[178:179], v196 offset:16384
	ds_read_b64_tr_b16 v[180:181], v197 offset:16384
	ds_read_b64_tr_b16 v[184:185], v197 offset:20480
	ds_read_b64_tr_b16 v[182:183], v196 offset:20480
	ds_read_b64_tr_b16 v[186:187], v202 offset:16384
	ds_read_b64_tr_b16 v[188:189], v203 offset:16384
	ds_read_b64_tr_b16 v[192:193], v203 offset:20480
	ds_read_b64_tr_b16 v[190:191], v202 offset:20480
	v_cndmask_b32_e64 v68, v165, 0, s[36:37]
	v_sub_f32_e32 v68, v68, v167
	v_mov_b32_e32 v82, v68
	v_mov_b32_e32 v83, v68
	v_mov_b32_e32 v69, v68
	v_mov_b32_e32 v70, v68
	v_mov_b32_e32 v71, v68
	v_mov_b32_e32 v72, v68
	v_mov_b32_e32 v73, v68
	v_mov_b32_e32 v74, v68
	v_mov_b32_e32 v75, v68
	v_mov_b32_e32 v76, v68
	v_mov_b32_e32 v77, v68
	v_mov_b32_e32 v78, v68
	v_mov_b32_e32 v79, v68
	v_mov_b32_e32 v80, v68
	v_mov_b32_e32 v81, v68
	s_nop 1
	s_waitcnt lgkmcnt(11)
	v_mfma_f32_32x32x16_bf16 v[100:115], v[204:207], v[116:119], v[68:83]
	s_waitcnt lgkmcnt(10)
	v_mfma_f32_32x32x16_bf16 v[84:99], v[208:211], v[116:119], v[68:83]
	s_waitcnt lgkmcnt(9)
	v_mfma_f32_32x32x16_bf16 v[100:115], v[212:215], v[120:123], v[100:115]
	ds_read_b128 v[204:207], v221
	ds_read_b128 v[208:211], v221 offset:4096
	ds_read_b128 v[212:215], v222
	s_waitcnt lgkmcnt(11)
	v_mfma_f32_32x32x16_bf16 v[84:99], v[216:219], v[120:123], v[84:99]
	ds_read_b128 v[216:219], v222 offset:4096
	s_waitcnt lgkmcnt(3)
	v_mfma_f32_32x32x16_bf16 v[100:115], v[204:207], v[124:127], v[100:115]
	s_waitcnt lgkmcnt(2)
	v_mfma_f32_32x32x16_bf16 v[84:99], v[208:211], v[124:127], v[84:99]
	s_waitcnt lgkmcnt(1)
	v_mfma_f32_32x32x16_bf16 v[68:83], v[212:215], v[128:131], v[100:115]
	s_waitcnt lgkmcnt(0)
	v_mfma_f32_32x32x16_bf16 v[84:99], v[216:219], v[128:131], v[84:99]
	s_andn2_b64 vcc, exec, s[36:37]
	s_cbranch_vccz .Latt_near

.Latt_near:
	v_add_u32_e32 v177, s5, v176
	s_mov_b32 s100, 0x207a4
	v_lshl_add_u32 v177, v177, 2, s100
	ds_read2_b32 v[204:205], v177 offset0:55 offset1:54
	ds_read2_b32 v[206:207], v177 offset0:53 offset1:52
	ds_read2_b32 v[208:209], v177 offset0:51 offset1:50
	ds_read2_b32 v[210:211], v177 offset0:49 offset1:48
	ds_read2_b32 v[212:213], v177 offset0:39 offset1:38
	ds_read2_b32 v[214:215], v177 offset0:37 offset1:36
	ds_read2_b32 v[216:217], v177 offset0:35 offset1:34
	ds_read2_b32 v[218:219], v177 offset0:33 offset1:32
	ds_read2_b32 v[220:221], v177 offset0:23 offset1:22
	ds_read2_b32 v[222:223], v177 offset0:21 offset1:20
	ds_read2_b32 v[224:225], v177 offset0:19 offset1:18
	ds_read2_b32 v[226:227], v177 offset0:17 offset1:16
	ds_read2_b32 v[228:229], v177 offset0:7 offset1:6
	ds_read2_b32 v[230:231], v177 offset0:5 offset1:4
	ds_read2_b32 v[232:233], v177 offset0:3 offset1:2
	s_waitcnt lgkmcnt(14)
	v_pk_add_f32 v[68:69], v[68:69], v[204:205]
	ds_read2_b32 v[204:205], v177 offset0:1 offset1:0
	s_waitcnt lgkmcnt(8)
	v_pk_add_f32 v[70:71], v[70:71], v[206:207]
	v_pk_add_f32 v[72:73], v[72:73], v[208:209]
	v_pk_add_f32 v[74:75], v[74:75], v[210:211]
	v_pk_add_f32 v[76:77], v[76:77], v[212:213]
	v_pk_add_f32 v[78:79], v[78:79], v[214:215]
	v_pk_add_f32 v[80:81], v[80:81], v[216:217]
	v_pk_add_f32 v[82:83], v[82:83], v[218:219]
	s_waitcnt lgkmcnt(0)
	v_pk_add_f32 v[84:85], v[84:85], v[220:221]
	v_pk_add_f32 v[86:87], v[86:87], v[222:223]
	v_pk_add_f32 v[88:89], v[88:89], v[224:225]
	v_pk_add_f32 v[90:91], v[90:91], v[226:227]
	v_pk_add_f32 v[92:93], v[92:93], v[228:229]
	v_pk_add_f32 v[94:95], v[94:95], v[230:231]
	v_pk_add_f32 v[96:97], v[96:97], v[232:233]
	v_pk_add_f32 v[98:99], v[98:99], v[204:205]
	s_branch .LBB0_432
.Latt_resc:
	v_max_f32_e32 v100, v69, v69
	v_max_f32_e32 v101, v68, v68
	v_max_f32_e32 v100, v101, v100
	v_max_f32_e32 v101, v71, v71
	v_max_f32_e32 v102, v70, v70
	v_max_f32_e32 v101, v102, v101
	v_max_f32_e32 v102, v75, v75
	v_max_f32_e32 v103, v74, v74
	v_max_f32_e32 v102, v103, v102
	v_max3_f32 v102, v72, v73, v102
	v_max3_f32 v100, v100, v101, v102
	v_max_f32_e32 v101, v77, v77
	v_max_f32_e32 v102, v76, v76
	v_max_f32_e32 v101, v102, v101
	v_max_f32_e32 v102, v79, v79
	v_max_f32_e32 v103, v78, v78
	v_max_f32_e32 v102, v103, v102
	v_max_f32_e32 v103, v83, v83
	v_max_f32_e32 v104, v82, v82
	v_max_f32_e32 v103, v104, v103
	v_max3_f32 v103, v80, v81, v103
	v_max3_f32 v101, v101, v102, v103
	v_max_f32_e32 v102, v87, v87
	v_max_f32_e32 v103, v86, v86
	v_max_f32_e32 v102, v103, v102
	v_max_f32_e32 v103, v91, v91
	v_max_f32_e32 v104, v90, v90
	v_max_f32_e32 v103, v104, v103
	v_max_f32_e32 v104, v93, v93
	v_max_f32_e32 v105, v92, v92
	v_max_f32_e32 v104, v105, v104
	v_max_f32_e32 v105, v95, v95
	v_max_f32_e32 v106, v94, v94
	v_max_f32_e32 v105, v106, v105
	v_max_f32_e32 v106, v99, v99
	v_max_f32_e32 v107, v98, v98
	v_max_f32_e32 v106, v107, v106
	v_max3_f32 v106, v96, v97, v106
	v_max3_f32 v102, v84, v85, v102
	v_max3_f32 v103, v88, v89, v103
	v_max3_f32 v104, v104, v105, v106
	v_max3_f32 v102, v102, v103, v104
	v_max3_f32 v100, v100, v101, v102
	v_mov_b32_e32 v101, v100
	s_nop 1
	v_permlane32_swap_b32 v101, v100
	s_nop 1
	s_nop 0
	v_max3_f32 v101, v101, v100, 1.0
	v_rcp_f32_e32 v100, v101
	s_nop 0
	v_pk_mul_f32 v[66:67], v[66:67], v[100:101] op_sel_hi:[1,0]
	v_pk_mul_f32 v[64:65], v[64:65], v[100:101] op_sel_hi:[1,0]
	v_pk_mul_f32 v[62:63], v[62:63], v[100:101] op_sel_hi:[1,0]
	v_pk_mul_f32 v[60:61], v[60:61], v[100:101] op_sel_hi:[1,0]
	v_pk_mul_f32 v[58:59], v[58:59], v[100:101] op_sel_hi:[1,0]
	v_pk_mul_f32 v[56:57], v[56:57], v[100:101] op_sel_hi:[1,0]
	v_pk_mul_f32 v[54:55], v[54:55], v[100:101] op_sel_hi:[1,0]
	v_pk_mul_f32 v[52:53], v[52:53], v[100:101] op_sel_hi:[1,0]
	v_pk_mul_f32 v[50:51], v[50:51], v[100:101] op_sel_hi:[1,0]
	v_pk_mul_f32 v[48:49], v[48:49], v[100:101] op_sel_hi:[1,0]
	v_pk_mul_f32 v[46:47], v[46:47], v[100:101] op_sel_hi:[1,0]
	v_pk_mul_f32 v[44:45], v[44:45], v[100:101] op_sel_hi:[1,0]
	v_pk_mul_f32 v[42:43], v[42:43], v[100:101] op_sel_hi:[1,0]
	v_pk_mul_f32 v[40:41], v[40:41], v[100:101] op_sel_hi:[1,0]
	v_pk_mul_f32 v[38:39], v[38:39], v[100:101] op_sel_hi:[1,0]
	v_pk_mul_f32 v[36:37], v[36:37], v[100:101] op_sel_hi:[1,0]
	v_pk_mul_f32 v[34:35], v[34:35], v[100:101] op_sel_hi:[1,0]
	v_pk_mul_f32 v[32:33], v[32:33], v[100:101] op_sel_hi:[1,0]
	v_pk_mul_f32 v[30:31], v[30:31], v[100:101] op_sel_hi:[1,0]
	v_pk_mul_f32 v[28:29], v[28:29], v[100:101] op_sel_hi:[1,0]
	v_pk_mul_f32 v[26:27], v[26:27], v[100:101] op_sel_hi:[1,0]
	v_pk_mul_f32 v[24:25], v[24:25], v[100:101] op_sel_hi:[1,0]
	v_pk_mul_f32 v[22:23], v[22:23], v[100:101] op_sel_hi:[1,0]
	v_pk_mul_f32 v[20:21], v[20:21], v[100:101] op_sel_hi:[1,0]
	v_pk_mul_f32 v[18:19], v[18:19], v[100:101] op_sel_hi:[1,0]
	v_pk_mul_f32 v[16:17], v[16:17], v[100:101] op_sel_hi:[1,0]
	v_pk_mul_f32 v[14:15], v[14:15], v[100:101] op_sel_hi:[1,0]
	v_pk_mul_f32 v[12:13], v[12:13], v[100:101] op_sel_hi:[1,0]
	v_pk_mul_f32 v[10:11], v[10:11], v[100:101] op_sel_hi:[1,0]
	v_pk_mul_f32 v[8:9], v[8:9], v[100:101] op_sel_hi:[1,0]
	v_pk_mul_f32 v[6:7], v[6:7], v[100:101] op_sel_hi:[1,0]
	v_pk_mul_f32 v[4:5], v[4:5], v[100:101] op_sel_hi:[1,0]
	v_log_f32_e32 v101, v101
	s_nop 0
	v_pk_mul_f32 v[82:83], v[82:83], v[100:101] op_sel_hi:[1,0]
	v_pk_mul_f32 v[80:81], v[80:81], v[100:101] op_sel_hi:[1,0]
	v_pk_mul_f32 v[78:79], v[78:79], v[100:101] op_sel_hi:[1,0]
	v_pk_mul_f32 v[76:77], v[76:77], v[100:101] op_sel_hi:[1,0]
	v_pk_mul_f32 v[74:75], v[74:75], v[100:101] op_sel_hi:[1,0]
	v_pk_mul_f32 v[72:73], v[72:73], v[100:101] op_sel_hi:[1,0]
	v_pk_mul_f32 v[70:71], v[70:71], v[100:101] op_sel_hi:[1,0]
	v_pk_mul_f32 v[68:69], v[68:69], v[100:101] op_sel_hi:[1,0]
	v_pk_mul_f32 v[98:99], v[98:99], v[100:101] op_sel_hi:[1,0]
	v_pk_mul_f32 v[96:97], v[96:97], v[100:101] op_sel_hi:[1,0]
	v_pk_mul_f32 v[94:95], v[94:95], v[100:101] op_sel_hi:[1,0]
	v_pk_mul_f32 v[92:93], v[92:93], v[100:101] op_sel_hi:[1,0]
	v_pk_mul_f32 v[90:91], v[90:91], v[100:101] op_sel_hi:[1,0]
	v_pk_mul_f32 v[88:89], v[88:89], v[100:101] op_sel_hi:[1,0]
	v_pk_mul_f32 v[86:87], v[86:87], v[100:101] op_sel_hi:[1,0]
	v_pk_mul_f32 v[84:85], v[84:85], v[100:101] op_sel_hi:[1,0]
	v_add_f32_e32 v167, v167, v101
	v_pk_mul_f32 v[152:153], v[152:153], v[100:101] op_sel_hi:[1,0]
	s_branch .LBB0_438

.LBB0_436:
	v_add_f32_e32 v100, v68, v84
	v_add_f32_e32 v100, 0, v100
	v_add_f32_e32 v101, v69, v85
	v_add_f32_e32 v100, v101, v100
	v_add_f32_e32 v101, v70, v86
	v_add_f32_e32 v100, v101, v100
	v_add_f32_e32 v101, v71, v87
	v_add_f32_e32 v112, v101, v100
	v_add_f32_e32 v110, v72, v88
	v_add_f32_e32 v111, v73, v89
	v_add_f32_e32 v108, v74, v90
	v_add_f32_e32 v109, v75, v91
	v_add_f32_e32 v110, v110, v112
	v_add_f32_e32 v110, v111, v110
	v_add_f32_e32 v108, v108, v110
	v_add_f32_e32 v106, v76, v92
	v_add_f32_e32 v107, v77, v93
	v_add_f32_e32 v108, v109, v108
	v_add_f32_e32 v106, v106, v108
	v_add_f32_e32 v104, v78, v94
	v_add_f32_e32 v105, v79, v95
	v_add_f32_e32 v106, v107, v106
	v_add_f32_e32 v104, v104, v106
	v_add_f32_e32 v102, v80, v96
	v_add_f32_e32 v103, v81, v97
	v_add_f32_e32 v104, v105, v104
	v_add_f32_e32 v102, v102, v104
	v_add_f32_e32 v100, v82, v98
	v_add_f32_e32 v101, v83, v99
	v_add_f32_e32 v102, v103, v102
	v_add_f32_e32 v100, v100, v102
	v_add_f32_e32 v152, v101, v100
	s_mov_b32 s0, 0x46000000
	v_cmp_nge_f32_e32 vcc, s0, v152
	s_cbranch_vccnz .Latt_resc
